# v9 + P2 conversion split rebalanced: cvA 15*2048 -> 7*2048 (10-unit WGs convert fewer items, 9-unit WGs more)
# baseline (speedup 1.0000x reference)
.LBB0_376:
	s_andn2_b64 vcc, exec, s[8:9]
	s_cbranch_vccnz .LBB0_599
	s_cmpk_eq_i32 s52, 0x100
	s_cselect_b64 s[0:1], -1, 0
	s_movk_i32 s10, 0x3800
	s_and_b64 s[8:9], s[0:1], exec
	s_cselect_b32 s21, s10, 0x8200
	s_lshl_b32 s8, s86, 3
	s_add_i32 s57, s8, s88
	s_mul_i32 s8, s88, 0x4100
	s_add_i32 s20, s8, 0
	s_cmp_ge_i32 s57, s21
	s_waitcnt vmcnt(0)
	s_barrier
	s_cbranch_scc1 .LBB0_486
	s_ashr_i32 s8, s57, 9
	s_mulk_i32 s8, 0x300
	s_and_b32 s16, s57, 0x1ff
	s_add_i32 s17, s8, s16
	s_addk_i32 s17, 0x3000
	s_cmpk_gt_i32 s17, 0x25ff
	s_cbranch_scc0 .LBB0_385
	s_cmpk_gt_u32 s17, 0x27ff
	s_cbranch_scc0 .LBB0_386
	s_cmpk_gt_u32 s17, 0x2bff
	s_cbranch_scc0 .LBB0_387
	s_cmpk_gt_u32 s17, 0x2fff
	s_cbranch_scc0 .LBB0_388
	s_add_i32 s18, s17, 0xffffd000
	s_and_b32 s8, s18, 0xffff
	s_mul_i32 s8, s8, 0xaaab
	s_lshr_b32 s14, s8, 25
	s_mul_i32 s8, s14, 0x300
	s_sub_i32 s8, s18, s8
	s_and_b32 s15, s8, 0xffff
	s_cmpk_gt_u32 s15, 0x1ff
	s_cbranch_scc0 .LBB0_389
	s_cmpk_gt_u32 s18, 0xbfff
	s_cbranch_scc0 .LBB0_390
	s_add_i32 s8, 0, 0x27ea8
	v_mov_b32_e32 v2, s8
	ds_read_b64 v[2:3], v2
	s_mov_b64 s[10:11], 0
	s_waitcnt lgkmcnt(0)
	v_readfirstlane_b32 s8, v2
	v_readfirstlane_b32 s9, v3
	s_branch .LBB0_391

.LBB0_486:
	s_cmpk_lt_i32 s90, 0x80
	s_cselect_b64 s[8:9], -1, 0
	s_xor_b64 s[0:1], s[0:1], -1
	s_or_b64 s[0:1], s[8:9], s[0:1]
	s_and_b64 vcc, exec, s[0:1]
	s_cbranch_vccnz .LBB0_598
	s_lshl_b32 s14, s90, 3
	s_add_i32 s14, s14, s88
	s_add_i32 s17, s14, 0xfffffc00
	s_cmpk_gt_i32 s17, 0x49ff
	s_cbranch_scc1 .LBB0_598
	s_add_i32 s0, s17, 0x3800
	s_ashr_i32 s0, s0, 9
	s_and_b32 s15, s17, 0x1ff
	s_mul_i32 s16, s0, 0x300
	s_or_b32 s18, s15, 0x3000
	s_add_i32 s16, s16, s18
	s_cmpk_gt_i32 s16, 0x25ff
	s_cbranch_scc0 .LBB0_495
	s_cmpk_gt_u32 s16, 0x27ff
	s_cbranch_scc0 .LBB0_496
	s_cmpk_gt_u32 s16, 0x2bff
	s_cbranch_scc0 .LBB0_497
	s_cmpk_gt_u32 s16, 0x2fff
	s_cbranch_scc0 .LBB0_498
	s_add_i32 s19, s16, 0xffffd000
	s_and_b32 s0, s19, 0xffff
	s_mul_i32 s0, s0, 0xaaab
	s_lshr_b32 s12, s0, 25
	s_mul_i32 s0, s12, 0x300
	s_sub_i32 s0, s19, s0
	s_and_b32 s13, s0, 0xffff
	s_cmpk_gt_u32 s13, 0x1ff
	s_cbranch_scc0 .LBB0_499
	s_cmpk_gt_u32 s19, 0xbfff
	s_cbranch_scc0 .LBB0_500
	s_add_i32 s0, 0, 0x27ea8
	s_waitcnt vmcnt(15)
	v_mov_b32_e32 v2, s0
	ds_read_b64 v[2:3], v2
	s_mov_b64 s[8:9], 0
	s_waitcnt lgkmcnt(0)
	v_readfirstlane_b32 s0, v2
	v_readfirstlane_b32 s1, v3
	s_branch .LBB0_501

.LBB0_524:
	v_lshrrev_b32_e32 v131, 4, v196
	s_waitcnt vmcnt(15)
	v_mul_u32_u24_e32 v2, s10, v131
	v_and_b32_e32 v130, 60, v204
	v_mov_b32_e32 v133, 0
	s_waitcnt lgkmcnt(0)
	v_lshlrev_b32_e32 v132, 2, v2
	v_lshl_add_u64 v[2:3], s[8:9], 0, v[132:133]
	v_lshlrev_b32_e32 v132, 2, v130
	v_or_b32_e32 v135, 4, v131
	s_waitcnt vmcnt(13)
	v_lshl_add_u64 v[10:11], v[2:3], 0, v[132:133]
	v_mul_u32_u24_e32 v2, s10, v135
	v_lshlrev_b32_e32 v2, 2, v2
	v_mov_b32_e32 v3, v133
	v_lshl_add_u64 v[2:3], s[8:9], 0, v[2:3]
	v_or_b32_e32 v139, 8, v131
	v_lshl_add_u64 v[12:13], v[2:3], 0, v[132:133]
	global_load_dwordx4 v[2:5], v[10:11], off
	global_load_dwordx4 v[6:9], v[12:13], off
	v_mul_u32_u24_e32 v10, s10, v139
	v_lshlrev_b32_e32 v10, 2, v10
	v_mov_b32_e32 v11, v133
	v_lshl_add_u64 v[10:11], s[8:9], 0, v[10:11]
	v_or_b32_e32 v141, 12, v131
	s_waitcnt vmcnt(13)
	v_lshl_add_u64 v[18:19], v[10:11], 0, v[132:133]
	v_mul_u32_u24_e32 v10, s10, v141
	v_lshlrev_b32_e32 v10, 2, v10
	v_mov_b32_e32 v11, v133
	v_lshl_add_u64 v[10:11], s[8:9], 0, v[10:11]
	v_or_b32_e32 v143, 16, v131
	v_lshl_add_u64 v[20:21], v[10:11], 0, v[132:133]
	global_load_dwordx4 v[10:13], v[18:19], off
	global_load_dwordx4 v[14:17], v[20:21], off
	v_mul_u32_u24_e32 v18, s10, v143
	v_lshlrev_b32_e32 v18, 2, v18
	v_mov_b32_e32 v19, v133
	v_lshl_add_u64 v[18:19], s[8:9], 0, v[18:19]
	v_or_b32_e32 v145, 20, v131
	s_waitcnt vmcnt(13)
	v_lshl_add_u64 v[26:27], v[18:19], 0, v[132:133]
	v_mul_u32_u24_e32 v18, s10, v145
	v_lshlrev_b32_e32 v18, 2, v18
	v_mov_b32_e32 v19, v133
	v_lshl_add_u64 v[18:19], s[8:9], 0, v[18:19]
	v_or_b32_e32 v147, 24, v131
	v_lshl_add_u64 v[28:29], v[18:19], 0, v[132:133]
	global_load_dwordx4 v[18:21], v[26:27], off
	global_load_dwordx4 v[22:25], v[28:29], off
	v_mul_u32_u24_e32 v26, s10, v147
	v_lshlrev_b32_e32 v26, 2, v26
	v_mov_b32_e32 v27, v133
	v_lshl_add_u64 v[26:27], s[8:9], 0, v[26:27]
	v_or_b32_e32 v149, 28, v131
	s_waitcnt vmcnt(13)
	v_lshl_add_u64 v[34:35], v[26:27], 0, v[132:133]
	v_mul_u32_u24_e32 v26, s10, v149
	v_lshlrev_b32_e32 v26, 2, v26
	v_mov_b32_e32 v27, v133
	v_lshl_add_u64 v[26:27], s[8:9], 0, v[26:27]
	v_or_b32_e32 v151, 32, v131
	v_lshl_add_u64 v[36:37], v[26:27], 0, v[132:133]
	global_load_dwordx4 v[26:29], v[34:35], off
	global_load_dwordx4 v[30:33], v[36:37], off
	v_mul_u32_u24_e32 v34, s10, v151
	v_lshlrev_b32_e32 v34, 2, v34
	v_mov_b32_e32 v35, v133
	v_lshl_add_u64 v[34:35], s[8:9], 0, v[34:35]
	v_or_b32_e32 v163, 36, v131
	s_waitcnt vmcnt(13)
	v_lshl_add_u64 v[42:43], v[34:35], 0, v[132:133]
	v_mul_u32_u24_e32 v34, s10, v163
	v_lshlrev_b32_e32 v34, 2, v34
	v_mov_b32_e32 v35, v133
	v_lshl_add_u64 v[34:35], s[8:9], 0, v[34:35]
	v_or_b32_e32 v165, 40, v131
	v_lshl_add_u64 v[44:45], v[34:35], 0, v[132:133]
	global_load_dwordx4 v[34:37], v[42:43], off
	global_load_dwordx4 v[38:41], v[44:45], off
	v_mul_u32_u24_e32 v42, s10, v165
	v_lshlrev_b32_e32 v42, 2, v42
	v_mov_b32_e32 v43, v133
	v_lshl_add_u64 v[42:43], s[8:9], 0, v[42:43]
	v_or_b32_e32 v167, 44, v131
	s_waitcnt vmcnt(13)
	v_lshl_add_u64 v[50:51], v[42:43], 0, v[132:133]
	v_mul_u32_u24_e32 v42, s10, v167
	v_lshlrev_b32_e32 v42, 2, v42
	v_mov_b32_e32 v43, v133
	v_lshl_add_u64 v[42:43], s[8:9], 0, v[42:43]
	v_or_b32_e32 v169, 48, v131
	v_lshl_add_u64 v[52:53], v[42:43], 0, v[132:133]
	global_load_dwordx4 v[42:45], v[50:51], off
	global_load_dwordx4 v[46:49], v[52:53], off
	v_mul_u32_u24_e32 v50, s10, v169
	v_lshlrev_b32_e32 v50, 2, v50
	v_mov_b32_e32 v51, v133
	v_lshl_add_u64 v[50:51], s[8:9], 0, v[50:51]
	v_or_b32_e32 v171, 52, v131
	v_lshl_add_u64 v[58:59], v[50:51], 0, v[132:133]
	v_mul_u32_u24_e32 v50, s10, v171
	v_lshlrev_b32_e32 v50, 2, v50
	v_mov_b32_e32 v51, v133
	v_lshl_add_u64 v[50:51], s[8:9], 0, v[50:51]
	v_or_b32_e32 v180, 56, v131
	v_lshl_add_u64 v[60:61], v[50:51], 0, v[132:133]
	global_load_dwordx4 v[50:53], v[58:59], off
	global_load_dwordx4 v[54:57], v[60:61], off
	v_mul_u32_u24_e32 v58, s10, v180
	v_or_b32_e32 v181, 60, v131
	v_lshlrev_b32_e32 v58, 2, v58
	v_mov_b32_e32 v59, v133
	v_mul_u32_u24_e32 v60, s10, v181
	v_lshl_add_u64 v[58:59], s[8:9], 0, v[58:59]
	v_lshlrev_b32_e32 v60, 2, v60
	v_mov_b32_e32 v61, v133
	v_lshl_add_u64 v[58:59], v[58:59], 0, v[132:133]
	v_lshl_add_u64 v[60:61], s[8:9], 0, v[60:61]
	v_lshl_add_u64 v[60:61], v[60:61], 0, v[132:133]
	global_load_dwordx4 v[74:77], v[58:59], off
	global_load_dwordx4 v[78:81], v[60:61], off
	s_lshl_b32 s8, s15, 5
	s_and_b32 s22, s8, 0xc0
	s_lshl_b32 s8, s15, 6
	s_bfe_u32 s21, s87, 0x10006
	s_and_b32 s23, s8, 64
	s_add_u32 s25, s50, 0x14400000
	s_addc_u32 s26, s51, 0
	s_add_u32 s27, s50, 0x4000000
	s_addc_u32 s28, s51, 0
	s_add_u32 s29, s50, 0x1600000
	s_addc_u32 s30, s51, 0
	s_add_u32 s31, s50, 0xe00000
	s_addc_u32 s33, s51, 0
	v_and_b32_e32 v60, 7, v0
	v_lshrrev_b32_e32 v134, 3, v196
	v_add_u32_e32 v58, s20, v132
	v_mul_u32_u24_e32 v59, 0x104, v131
	s_add_u32 s34, s50, 0xa00000
	v_mul_u32_u24_e32 v61, 0x820, v60
	v_lshlrev_b32_e32 v62, 2, v134
	s_addc_u32 s35, s51, 0
	v_lshlrev_b32_e32 v136, 3, v60
	v_mov_b32_e32 v137, v133
	v_add3_u32 v182, s20, v61, v62
	v_or_b32_e32 v138, 8, v134
	v_or_b32_e32 v140, 16, v134
	v_or_b32_e32 v142, 24, v134
	v_or_b32_e32 v144, 32, v134
	v_or_b32_e32 v146, 40, v134
	v_or_b32_e32 v148, 48, v134
	v_or_b32_e32 v150, 56, v134
	v_lshlrev_b32_e32 v152, 4, v60
	v_mov_b32_e32 v153, v133
	s_add_i32 s57, s14, 0x2c00
	s_add_i32 s20, 0, 0x27ea8
	s_add_i32 s37, 0, 0x27e90
	s_movk_i32 s42, 0x98
	s_movk_i32 s43, 0x88
	s_add_i32 s44, 0, 0x27e60
	s_add_i32 s45, 0, 0x27e58
	s_add_i32 s46, 0, 0x27e50
	s_add_i32 s47, 0, 0x27e30
	s_mov_b32 s53, 0xc3e00000
	v_add_u32_e32 v183, v58, v59
	v_mov_b32_e32 v184, 0x43e00000
	s_mov_b32 s56, s24
	s_mov_b32 s55, s19
	s_mov_b64 s[8:9], s[0:1]
	s_branch .LBB0_528
